# v50 with spacer lengths A=3 B=2 (x64 cycles) after the sub-head-0 softmax
# baseline (speedup 1.0000x reference)
.LBB0_215:
	v_add_u32_e32 v212, s56, v225
	v_add_u32_e32 v6, v212, v227
	v_add_u32_e32 v7, v212, v228
	ds_read_b128 v[244:247], v6
	ds_read_b128 v[248:251], v6 offset:8192
	ds_read_b128 v[236:239], v7
	ds_read_b128 v[240:243], v7 offset:8192
	v_add_u32_e32 v6, v212, v229
	v_add_u32_e32 v7, v212, v230
	ds_read_b128 v[2:5], v6
	ds_read_b128 v[8:11], v6 offset:8192
	ds_read_b128 v[208:211], v7
	s_xor_b64 s[44:45], s[44:45], -1
	v_add_u32_e32 v6, v212, v226
	s_waitcnt lgkmcnt(6)
	v_mfma_f32_32x32x16_bf16 v[160:175], v[244:247], v[176:179], v[160:175]
	ds_read_b128 v[244:247], v7 offset:8192
	s_waitcnt lgkmcnt(6)
	v_mfma_f32_32x32x16_bf16 v[144:159], v[248:251], v[176:179], v[144:159]
	s_waitcnt lgkmcnt(5)
	v_mfma_f32_32x32x16_bf16 v[160:175], v[236:239], v[180:183], v[160:175]
	v_add_u32_e32 v7, v212, v231
	s_waitcnt lgkmcnt(4)
	v_mfma_f32_32x32x16_bf16 v[144:159], v[240:243], v[180:183], v[144:159]
	ds_read_b128 v[248:251], v6
	ds_read_b128 v[236:239], v6 offset:8192
	ds_read_b128 v[240:243], v7
	s_waitcnt lgkmcnt(6)
	v_mfma_f32_32x32x16_bf16 v[160:175], v[2:5], v[184:187], v[160:175]
	s_waitcnt lgkmcnt(5)
	v_mfma_f32_32x32x16_bf16 v[144:159], v[8:11], v[184:187], v[144:159]
	s_waitcnt lgkmcnt(4)
	v_mfma_f32_32x32x16_bf16 v[160:175], v[208:211], v[188:191], v[160:175]
	s_waitcnt lgkmcnt(3)
	v_mfma_f32_32x32x16_bf16 v[144:159], v[244:247], v[188:191], v[144:159]
	ds_read_b128 v[244:247], v7 offset:8192
	s_nop 9
	v_exp_f32_e32 v6, v160
	v_exp_f32_e32 v3, v161
	v_exp_f32_e32 v10, v164
	v_exp_f32_e32 v11, v165
	v_exp_f32_e32 v160, v172
	v_exp_f32_e32 v161, v173
	v_exp_f32_e32 v5, v162
	v_exp_f32_e32 v2, v144
	v_exp_f32_e32 v7, v146
	v_exp_f32_e32 v144, v148
	v_exp_f32_e32 v146, v150
	v_exp_f32_e32 v148, v168
	v_exp_f32_e32 v150, v169
	v_exp_f32_e32 v4, v145
	v_exp_f32_e32 v145, v149
	v_exp_f32_e32 v12, v166
	v_exp_f32_e32 v149, v152
	v_exp_f32_e32 v152, v170
	v_exp_f32_e32 v162, v174
	v_exp_f32_e32 v8, v163
	v_exp_f32_e32 v9, v147
	v_exp_f32_e32 v13, v167
	v_exp_f32_e32 v147, v151
	v_exp_f32_e32 v151, v153
	v_exp_f32_e32 v153, v154
	v_exp_f32_e32 v154, v171
	v_exp_f32_e32 v163, v175
	v_exp_f32_e32 v156, v156
	v_exp_f32_e32 v157, v157
	v_add_f32_e32 v164, v6, v3
	v_add_f32_e32 v165, v10, v11
	v_add_f32_e32 v166, v148, v150
	v_add_f32_e32 v167, v160, v161
	v_exp_f32_e32 v158, v158
	v_add_f32_e32 v164, v5, v164
	v_add_f32_e32 v165, v12, v165
	v_add_f32_e32 v166, v152, v166
	v_add_f32_e32 v167, v162, v167
	v_exp_f32_e32 v155, v155
	v_exp_f32_e32 v159, v159
	v_add_f32_e32 v164, v8, v164
	v_add_f32_e32 v165, v13, v165
	v_add_f32_e32 v166, v154, v166
	v_add_f32_e32 v167, v163, v167
	v_add_f32_e32 v164, v2, v164
	v_add_f32_e32 v165, v144, v165
	v_add_f32_e32 v166, v149, v166
	v_add_f32_e32 v167, v156, v167
	v_add_f32_e32 v164, v4, v164
	v_add_f32_e32 v165, v145, v165
	v_add_f32_e32 v166, v151, v166
	v_add_f32_e32 v167, v157, v167
	v_add_f32_e32 v164, v7, v164
	v_add_f32_e32 v165, v146, v165
	v_add_f32_e32 v166, v153, v166
	v_add_f32_e32 v167, v158, v167
	v_add_f32_e32 v164, v9, v164
	v_add_f32_e32 v165, v147, v165
	v_add_f32_e32 v166, v155, v166
	v_add_f32_e32 v167, v159, v167
	v_add_f32_e32 v164, v164, v165
	v_add_f32_e32 v165, v166, v167
	v_add_f32_e32 v213, v164, v165
	v_mov_b32_e32 v218, v213
	v_cvt_pk_bf16_f32 v208, v6, v3
	v_cvt_pk_bf16_f32 v209, v5, v8
	v_cvt_pk_bf16_f32 v210, v10, v11
	v_cvt_pk_bf16_f32 v211, v12, v13
	v_cvt_pk_bf16_f32 v10, v148, v150
	v_cvt_pk_bf16_f32 v11, v152, v154
	v_cvt_pk_bf16_f32 v12, v160, v161
	v_cvt_pk_bf16_f32 v13, v162, v163
	v_cvt_pk_bf16_f32 v6, v2, v4
	v_cvt_pk_bf16_f32 v7, v7, v9
	v_cvt_pk_bf16_f32 v8, v144, v145
	v_cvt_pk_bf16_f32 v9, v146, v147
	v_cvt_pk_bf16_f32 v2, v149, v151
	v_cvt_pk_bf16_f32 v3, v153, v155
	v_cvt_pk_bf16_f32 v4, v156, v157
	v_cvt_pk_bf16_f32 v5, v158, v159
	v_permlane32_swap_b32_e32 v213, v218
	v_permlane32_swap_b32_e32 v208, v210
	v_permlane32_swap_b32_e32 v209, v211
	v_permlane32_swap_b32_e32 v10, v12
	v_permlane32_swap_b32_e32 v11, v13
	v_permlane32_swap_b32_e32 v6, v8
	v_permlane32_swap_b32_e32 v7, v9
	v_permlane32_swap_b32_e32 v2, v4
	v_permlane32_swap_b32_e32 v3, v5
	s_nop 15
	s_nop 15
	s_nop 15
	v_mov_b32_e32 v160, 0
	s_andn2_b64 vcc, exec, s[44:45]
	v_mov_b32_e32 v161, 0
	v_mov_b32_e32 v162, 0
	v_mov_b32_e32 v163, 0
	v_mov_b32_e32 v164, 0
	v_mov_b32_e32 v165, 0
	v_mov_b32_e32 v166, 0
	v_mov_b32_e32 v167, 0
	v_mov_b32_e32 v168, 0
	v_mov_b32_e32 v169, 0
	v_mov_b32_e32 v170, 0
	v_mov_b32_e32 v171, 0
	v_mov_b32_e32 v172, 0
	v_mov_b32_e32 v173, 0
	v_mov_b32_e32 v174, 0
	v_mov_b32_e32 v175, 0
	v_mov_b32_e32 v144, 0
	v_mov_b32_e32 v145, 0
	v_mov_b32_e32 v146, 0
	v_mov_b32_e32 v147, 0
	v_mov_b32_e32 v148, 0
	v_mov_b32_e32 v149, 0
	v_mov_b32_e32 v150, 0
	v_mov_b32_e32 v151, 0
	v_mov_b32_e32 v152, 0
	v_mov_b32_e32 v153, 0
	v_mov_b32_e32 v154, 0
	v_mov_b32_e32 v155, 0
	v_mov_b32_e32 v156, 0
	v_mov_b32_e32 v157, 0
	v_mov_b32_e32 v158, 0
	v_mov_b32_e32 v159, 0
	s_cbranch_vccnz .LBB0_205
	s_andn2_b64 vcc, exec, s[42:43]
	s_mov_b64 s[42:43], -1
	s_cbranch_vccnz .LBB0_218
	v_add_u32_e32 v146, 0x21780, v219
	v_add_u32_e32 v147, 0x21708, v219
	v_add_u32_e32 v148, 0x21788, v219
	ds_read2_b32 v[144:145], v220 offset1:1
	ds_read2_b32 v[160:161], v146 offset1:1
	ds_read2_b32 v[146:147], v147 offset1:1
	ds_read2_b32 v[162:163], v148 offset1:1
	v_add_u32_e32 v148, 0x21720, v219
	v_add_u32_e32 v150, 0x217a0, v219
	v_add_u32_e32 v151, 0x21728, v219
	v_add_u32_e32 v152, 0x217a8, v219
	ds_read2_b32 v[148:149], v148 offset1:1
	ds_read2_b32 v[164:165], v150 offset1:1
	ds_read2_b32 v[150:151], v151 offset1:1
	ds_read2_b32 v[166:167], v152 offset1:1
	v_add_u32_e32 v152, 0x21740, v219
	v_add_u32_e32 v154, 0x217c0, v219
	v_add_u32_e32 v155, 0x21748, v219
	v_add_u32_e32 v156, 0x217c8, v219
	ds_read2_b32 v[152:153], v152 offset1:1
	ds_read2_b32 v[168:169], v154 offset1:1
	ds_read2_b32 v[154:155], v155 offset1:1
	ds_read2_b32 v[170:171], v156 offset1:1
	v_add_u32_e32 v156, 0x21760, v219
	v_add_u32_e32 v158, 0x217e0, v219
	v_add_u32_e32 v159, 0x21768, v219
	v_add_u32_e32 v174, 0x217e8, v219
	ds_read2_b32 v[156:157], v156 offset1:1
	ds_read2_b32 v[172:173], v158 offset1:1
	ds_read2_b32 v[158:159], v159 offset1:1
	ds_read2_b32 v[174:175], v174 offset1:1
	s_mov_b64 s[42:43], 0
